# P1 epilogue: Z gate column tiles (read only in P7) stored nt, tiles re-read by P3-P5 keep default policy
# baseline (speedup 1.0000x reference)
;     __device__ __forceinline__ void operator()(const f32x4 (&acc)[2][2][4][2], const Unit& u, int wr, int wc, int fr, int fq) const {
;         const int row0 = u.pm * BM + wr * 64 + fr, col0 = u.pn * BM + wc * 32 + 8 * fq;
;         const float tsc = (MODE == 0 && u.pn >= sc_lo && u.pn < sc_hi) ? sc : 1.f;
;         float ra[2][4]; f32x4 cb[2][2];
;         if (QI8) {
; #pragma unroll
;             for (int ai = 0; ai < 2; ++ai)
; #pragma unroll
;                 for (int m = 0; m < 4; ++m) ra[ai][m] = sa[row0 + ai * HALF + m * 16];
; #pragma unroll
;             for (int bj = 0; bj < 2; ++bj) { cb[bj][0] = *(const f32x4*)(sb + col0 + bj * HALF) * tsc; cb[bj][1] = *(const f32x4*)(sb + col0 + bj * HALF + 4) * tsc; } }
;         else if (MODE == 1) {
; #pragma unroll
;             for (int bj = 0; bj < 2; ++bj) { cb[bj][0] = *(const f32x4*)(colscale + col0 + bj * HALF); cb[bj][1] = *(const f32x4*)(colscale + col0 + bj * HALF + 4); } }
;         const bool dual = (MODE == 0) && aux != nullptr && u.pn >= ZC_KV / 256 && u.pn < ZC_KV / 256 + 4;
;         u32x4 gq[2][2], aq[2][2]; f32x4 rs[2][2][2];
;     ...
;         EPB_LOAD(0);
; #pragma unroll
;         for (int kb = 0; kb < 8; ++kb) { const int ai = kb >> 2, m = kb & 3;
;             if (kb < 7) EPB_LOAD(kb + 1);
;             { const int row = row0 + ai * HALF + m * 16; float rmx = 0.f;
; #pragma unroll
;                 for (int bj = 0; bj < 2; ++bj) { const int col = col0 + bj * HALF; f32x4 v0 = acc[ai][bj][m][0], v1 = acc[ai][bj][m][1];
;                     if (QI8) { const f32x4 c0 = cb[bj][0] * ra[ai][m], c1 = cb[bj][1] * ra[ai][m]; const i32x4 i0 = __builtin_bit_cast(i32x4, v0), i1 = __builtin_bit_cast(i32x4, v1);
;                         v0 = (f32x4){(float)i0[0], (float)i0[1], (float)i0[2], (float)i0[3]} * c0; v1 = (f32x4){(float)i1[0], (float)i1[1], (float)i1[2], (float)i1[3]} * c1; }
;                     else if (MODE == 0) { v0 = v0 * tsc; v1 = v1 * tsc; }
;                     if (!QI8 && MODE == 1) { v0 = v0 * cb[bj][0]; v1 = v1 * cb[bj][1]; }
;                     if (MODE == 2 || MODE == 3) { const u32x4 g = gq[kb & 1][bj];
;                         f32x4 g0 = {sigmoidf_(bflo(g.x)), sigmoidf_(bfhi(g.x)), sigmoidf_(bflo(g.y)), sigmoidf_(bfhi(g.y))};
;                         f32x4 g1 = {sigmoidf_(bflo(g.z)), sigmoidf_(bfhi(g.z)), sigmoidf_(bflo(g.w)), sigmoidf_(bfhi(g.w))};
.LBB0_167:
	s_cmp_gt_u32 s30, 28
	s_cselect_b64 s[78:79], -1, 0
	s_cselect_b64 s[80:81], 0, -1
	v_lshl_or_b32 v138, s30, 8, v228
	v_ashrrev_i32_e32 v139, 31, v138
	v_lshl_add_u64 v[134:135], v[138:139], 2, s[16:17]
	global_load_dwordx4 v[166:169], v[134:135], off offset:16
	global_load_dwordx4 v[144:147], v[134:135], off
	s_lshl_b32 s10, s10, 8
	s_add_i32 s23, s10, s63
	v_or_b32_e32 v156, s23, v1
	v_ashrrev_i32_e32 v157, 31, v156
	v_lshl_add_u64 v[140:141], v[156:157], 2, s[4:5]
	global_load_dword v164, v[140:141], off
	global_load_dwordx4 v[130:133], v[134:135], off offset:528
	s_nop 0
	global_load_dwordx4 v[134:137], v[134:135], off offset:512
	s_nop 0
	global_load_dword v162, v[140:141], off offset:64
	global_load_dword v160, v[140:141], off offset:128
	global_load_dword v158, v[140:141], off offset:192
	global_load_dword v154, v[140:141], off offset:512
	global_load_dword v152, v[140:141], off offset:576
	global_load_dword v142, v[140:141], off offset:640
	s_nop 0
	global_load_dword v140, v[140:141], off offset:704
	s_and_b32 s10, s30, -8
	v_readlane_b32 s34, v245, 9
	s_cmp_eq_u32 s10, 8
	v_cvt_f32_i32_e32 v171, v129
	v_cvt_f32_i32_e32 v170, v128
	v_readlane_b32 s35, v245, 10
	s_cselect_b64 vcc, -1, 0
	v_cvt_f32_i32_e32 v127, v127
	v_cvt_f32_i32_e32 v126, v126
	v_cvt_f32_i32_e32 v123, v123
	v_cvt_f32_i32_e32 v122, v122
	v_cvt_f32_i32_e32 v125, v125
	v_cvt_f32_i32_e32 v124, v124
	v_mov_b64_e32 v[148:149], s[34:35]
	v_cndmask_b32_e32 v128, 1.0, v232, vcc
	s_and_b32 s25, s30, -4
	v_mad_i64_i32 v[172:173], s[10:11], v156, s68, v[148:149]
	s_cmp_eq_u32 s25, 16
	s_cselect_b64 s[34:35], -1, 0
	s_ashr_i32 s23, s23, 4
	s_addk_i32 s23, 0xc000
	s_cmp_lg_u32 s25, 16
	s_waitcnt vmcnt(0)
	v_pk_mul_f32 v[148:149], v[128:129], v[146:147] op_sel_hi:[0,1]
	v_pk_mul_f32 v[150:151], v[128:129], v[144:145] op_sel_hi:[0,1]
	v_pk_mul_f32 v[144:145], v[128:129], v[168:169] op_sel_hi:[0,1]
	v_pk_mul_f32 v[146:147], v[128:129], v[166:167] op_sel_hi:[0,1]
	v_pk_mul_f32 v[166:167], v[164:165], v[148:149] op_sel_hi:[0,1]
	v_pk_mul_f32 v[168:169], v[164:165], v[150:151] op_sel_hi:[0,1]
	v_pk_mul_f32 v[174:175], v[164:165], v[144:145] op_sel_hi:[0,1]
	v_pk_mul_f32 v[176:177], v[164:165], v[146:147] op_sel_hi:[0,1]
	v_pk_mul_f32 v[166:167], v[166:167], v[170:171]
	v_pk_mul_f32 v[126:127], v[168:169], v[126:127]
	v_pk_mul_f32 v[168:169], v[174:175], v[124:125]
	v_pk_mul_f32 v[124:125], v[176:177], v[122:123]
	v_cvt_pk_bf16_f32 v122, v126, v127
	v_cvt_pk_bf16_f32 v123, v166, v167
	v_lshl_add_u64 v[166:167], v[138:139], 1, v[172:173]
	v_cvt_pk_bf16_f32 v124, v124, v125
	v_cvt_pk_bf16_f32 v125, v168, v169
	s_mov_b64 exec, s[78:79]
	global_store_dwordx4 v[166:167], v[122:125], off nt
	s_mov_b64 exec, s[80:81]
	global_store_dwordx4 v[166:167], v[122:125], off
	s_mov_b64 exec, -1
	s_cbranch_scc1 .LBB0_169
	s_lshl_b32 s10, s30, 10
	s_add_i32 s10, s23, s10
	s_ashr_i32 s11, s10, 31
	s_lshl_b64 s[10:11], s[10:11], 12
	v_lshl_add_u64 v[126:127], v[206:207], 0, s[10:11]
	global_store_dwordx4 v[126:127], v[122:125], off
.LBB0_169:
	v_cvt_f32_i32_e32 v119, v119
	v_cvt_f32_i32_e32 v118, v118
	v_mov_b32_e32 v129, v128
	v_cvt_f32_i32_e32 v115, v115
	v_cvt_f32_i32_e32 v117, v117
	v_cvt_f32_i32_e32 v116, v116
	v_cvt_f32_i32_e32 v114, v114
	v_mov_b32_e32 v165, v164
	v_mov_b32_e32 v122, v128
	v_mov_b32_e32 v123, v128
	v_pk_mul_f32 v[126:127], v[128:129], v[134:135]
	v_pk_mul_f32 v[124:125], v[122:123], v[136:137]
	v_pk_mul_f32 v[122:123], v[122:123], v[132:133]
	v_pk_mul_f32 v[128:129], v[128:129], v[130:131]
	v_mov_b32_e32 v130, v164
	v_mov_b32_e32 v131, v164
	v_pk_mul_f32 v[134:135], v[164:165], v[126:127]
	v_pk_mul_f32 v[132:133], v[130:131], v[124:125]
	v_pk_mul_f32 v[130:131], v[130:131], v[122:123]
	v_pk_mul_f32 v[136:137], v[164:165], v[128:129]
	v_cvt_f32_i32_e32 v121, v121
	v_cvt_f32_i32_e32 v120, v120
	v_pk_mul_f32 v[118:119], v[134:135], v[118:119]
	v_or_b32_e32 v141, 0x80, v138
	v_pk_mul_f32 v[130:131], v[130:131], v[116:117]
	v_pk_mul_f32 v[116:117], v[136:137], v[114:115]
	v_cvt_pk_bf16_f32 v114, v118, v119
	v_cndmask_b32_e64 v118, 0, 1, s[34:35]
	v_cmp_ne_u32_e64 s[10:11], 1, v118
	v_lshlrev_b32_e32 v118, 2, v141
	s_andn2_b64 vcc, exec, s[34:35]
	v_and_b32_e32 v118, 0x4e00, v118
	v_pk_mul_f32 v[120:121], v[132:133], v[120:121]
	s_nop 0
	v_cvt_pk_bf16_f32 v115, v120, v121
	v_cvt_pk_bf16_f32 v116, v116, v117
	v_cvt_pk_bf16_f32 v117, v130, v131
	s_mov_b64 exec, s[78:79]
	global_store_dwordx4 v[166:167], v[114:117], off offset:256 nt
	s_mov_b64 exec, s[80:81]
	global_store_dwordx4 v[166:167], v[114:117], off offset:256
	s_mov_b64 exec, -1
	s_cbranch_vccnz .LBB0_171
	v_add_u32_e32 v120, s23, v118
	v_ashrrev_i32_e32 v121, 31, v120
	v_lshlrev_b64 v[120:121], 12, v[120:121]
	v_lshl_add_u64 v[120:121], v[206:207], 0, v[120:121]
	global_store_dwordx4 v[120:121], v[114:117], off
.LBB0_171:
	v_cvt_f32_i32_e32 v111, v111
	v_cvt_f32_i32_e32 v110, v110
	v_cvt_f32_i32_e32 v113, v113
	v_cvt_f32_i32_e32 v112, v112
	v_cvt_f32_i32_e32 v107, v107
	v_cvt_f32_i32_e32 v109, v109
	v_cvt_f32_i32_e32 v108, v108
	v_cvt_f32_i32_e32 v106, v106
	v_pk_mul_f32 v[120:121], v[162:163], v[150:151] op_sel_hi:[0,1]
	v_readlane_b32 s34, v245, 9
	v_pk_mul_f32 v[116:117], v[162:163], v[148:149] op_sel_hi:[0,1]
	v_pk_mul_f32 v[130:131], v[162:163], v[144:145] op_sel_hi:[0,1]
	v_pk_mul_f32 v[132:133], v[162:163], v[146:147] op_sel_hi:[0,1]
	v_pk_mul_f32 v[110:111], v[120:121], v[110:111]
	v_readlane_b32 s35, v245, 10
	v_or_b32_e32 v115, 16, v156
	v_pk_mul_f32 v[112:113], v[116:117], v[112:113]
	v_pk_mul_f32 v[116:117], v[130:131], v[108:109]
	v_pk_mul_f32 v[108:109], v[132:133], v[106:107]
	v_cvt_pk_bf16_f32 v106, v110, v111
	v_mov_b64_e32 v[110:111], s[34:35]
	v_ashrrev_i32_e32 v114, 4, v115
	v_mad_i64_i32 v[110:111], s[34:35], v115, s68, v[110:111]
	v_add_u32_e32 v114, 0xffffc000, v114
	v_lshl_add_u64 v[110:111], v[138:139], 1, v[110:111]
	s_and_b64 vcc, exec, s[10:11]
	v_cvt_pk_bf16_f32 v107, v112, v113
	v_cvt_pk_bf16_f32 v108, v108, v109
	v_cvt_pk_bf16_f32 v109, v116, v117
	s_mov_b64 exec, s[78:79]
	global_store_dwordx4 v[110:111], v[106:109], off nt
	s_mov_b64 exec, s[80:81]
	global_store_dwordx4 v[110:111], v[106:109], off
	s_mov_b64 exec, -1
	s_cbranch_vccnz .LBB0_173
	v_lshl_add_u32 v112, s30, 10, v114
	v_ashrrev_i32_e32 v113, 31, v112
	v_lshlrev_b64 v[112:113], 12, v[112:113]
	v_lshl_add_u64 v[112:113], v[206:207], 0, v[112:113]
	global_store_dwordx4 v[112:113], v[106:109], off
;     __device__ __forceinline__ void operator()(const f32x4 (&acc)[2][2][4][2], const Unit& u, int wr, int wc, int fr, int fq) const {
;     ...
;         for (int kb = 0; kb < 8; ++kb) { const int ai = kb >> 2, m = kb & 3;
;             if (kb < 7) EPB_LOAD(kb + 1);
;             { const int row = row0 + ai * HALF + m * 16; float rmx = 0.f;
; #pragma unroll
;                 for (int bj = 0; bj < 2; ++bj) { const int col = col0 + bj * HALF; f32x4 v0 = acc[ai][bj][m][0], v1 = acc[ai][bj][m][1];
;                     if (QI8) { const f32x4 c0 = cb[bj][0] * ra[ai][m], c1 = cb[bj][1] * ra[ai][m]; const i32x4 i0 = __builtin_bit_cast(i32x4, v0), i1 = __builtin_bit_cast(i32x4, v1);
;                         v0 = (f32x4){(float)i0[0], (float)i0[1], (float)i0[2], (float)i0[3]} * c0; v1 = (f32x4){(float)i1[0], (float)i1[1], (float)i1[2], (float)i1[3]} * c1; }
;                     else if (MODE == 0) { v0 = v0 * tsc; v1 = v1 * tsc; }
;                     if (!QI8 && MODE == 1) { v0 = v0 * cb[bj][0]; v1 = v1 * cb[bj][1]; }
;                     if (MODE == 2 || MODE == 3) { const u32x4 g = gq[kb & 1][bj];
;                         f32x4 g0 = {sigmoidf_(bflo(g.x)), sigmoidf_(bfhi(g.x)), sigmoidf_(bflo(g.y)), sigmoidf_(bfhi(g.y))};
;                         f32x4 g1 = {sigmoidf_(bflo(g.z)), sigmoidf_(bfhi(g.z)), sigmoidf_(bflo(g.w)), sigmoidf_(bfhi(g.w))};
;                         v0 = v0 * g0; v1 = v1 * g1;
;                         if (MODE == 3) { const u32x4 q = aq[kb & 1][bj];
;                             v0 = v0 + (f32x4){bflo(q.x), bfhi(q.x), bflo(q.y), bfhi(q.y)}; v1 = v1 + (f32x4){bflo(q.z), bfhi(q.z), bflo(q.w), bfhi(q.w)}; } }
;                     if (MODE == 4) { v0 = v0 + rs[kb & 1][bj][0]; v1 = v1 + rs[kb & 1][bj][1]; }
;                     if (MODE == 5) { const u32x4 c = gq[kb & 1][bj], q = aq[kb & 1][bj];
;                         v0 = (f32x4){bflo(c.x) + sigmoidf_(v0[0]) * bflo(q.x), bfhi(c.x) + sigmoidf_(v0[1]) * bfhi(q.x), bflo(c.y) + sigmoidf_(v0[2]) * bflo(q.y), bfhi(c.y) + sigmoidf_(v0[3]) * bfhi(q.y)};
;                         v1 = (f32x4){bflo(c.z) + sigmoidf_(v1[0]) * bflo(q.z), bfhi(c.z) + sigmoidf_(v1[1]) * bfhi(q.z), bflo(c.w) + sigmoidf_(v1[2]) * bflo(q.w), bfhi(c.w) + sigmoidf_(v1[3]) * bfhi(q.w)}; }
;                     u32x4 w; w.x = cvtpk(v0[0], v0[1]); w.y = cvtpk(v0[2], v0[3]); w.z = cvtpk(v1[0], v1[1]); w.w = cvtpk(v1[2], v1[3]);
.LBB0_173:
	v_cvt_f32_i32_e32 v99, v99
	v_cvt_f32_i32_e32 v101, v101
	v_cvt_f32_i32_e32 v100, v100
	v_cvt_f32_i32_e32 v98, v98
	v_cvt_f32_i32_e32 v103, v103
	v_cvt_f32_i32_e32 v102, v102
	v_cvt_f32_i32_e32 v105, v105
	v_cvt_f32_i32_e32 v104, v104
	v_mov_b32_e32 v163, v162
	v_mov_b32_e32 v106, v162
	v_mov_b32_e32 v107, v162
	v_pk_mul_f32 v[108:109], v[106:107], v[124:125]
	v_pk_mul_f32 v[106:107], v[106:107], v[122:123]
	v_pk_mul_f32 v[116:117], v[162:163], v[128:129]
	v_pk_mul_f32 v[112:113], v[162:163], v[126:127]
	v_pk_mul_f32 v[106:107], v[106:107], v[100:101]
	v_pk_mul_f32 v[100:101], v[116:117], v[98:99]
	s_and_b64 vcc, exec, s[10:11]
	v_pk_mul_f32 v[104:105], v[108:109], v[104:105]
	v_pk_mul_f32 v[102:103], v[112:113], v[102:103]
	s_nop 0
	v_cvt_pk_bf16_f32 v98, v102, v103
	v_cvt_pk_bf16_f32 v99, v104, v105
	v_cvt_pk_bf16_f32 v100, v100, v101
	v_cvt_pk_bf16_f32 v101, v106, v107
	s_mov_b64 exec, s[78:79]
	global_store_dwordx4 v[110:111], v[98:101], off offset:256 nt
	s_mov_b64 exec, s[80:81]
	global_store_dwordx4 v[110:111], v[98:101], off offset:256
	s_mov_b64 exec, -1
	s_cbranch_vccnz .LBB0_175
	v_add_u32_e32 v102, v114, v118
	v_ashrrev_i32_e32 v103, 31, v102
	v_lshlrev_b64 v[102:103], 12, v[102:103]
	v_lshl_add_u64 v[102:103], v[206:207], 0, v[102:103]
	global_store_dwordx4 v[102:103], v[98:101], off
.LBB0_175:
	v_cvt_f32_i32_e32 v95, v95
	v_cvt_f32_i32_e32 v94, v94
	v_cvt_f32_i32_e32 v97, v97
	v_cvt_f32_i32_e32 v96, v96
	v_cvt_f32_i32_e32 v91, v91
	v_cvt_f32_i32_e32 v93, v93
	v_cvt_f32_i32_e32 v92, v92
	v_cvt_f32_i32_e32 v90, v90
	v_pk_mul_f32 v[102:103], v[160:161], v[150:151] op_sel_hi:[0,1]
	v_readlane_b32 s34, v245, 9
	v_pk_mul_f32 v[100:101], v[160:161], v[148:149] op_sel_hi:[0,1]
	v_pk_mul_f32 v[104:105], v[160:161], v[144:145] op_sel_hi:[0,1]
	v_pk_mul_f32 v[106:107], v[160:161], v[146:147] op_sel_hi:[0,1]
	v_pk_mul_f32 v[94:95], v[102:103], v[94:95]
	v_readlane_b32 s35, v245, 10
	v_or_b32_e32 v99, 32, v156
	v_pk_mul_f32 v[96:97], v[100:101], v[96:97]
	v_pk_mul_f32 v[100:101], v[104:105], v[92:93]
	v_pk_mul_f32 v[92:93], v[106:107], v[90:91]
	v_cvt_pk_bf16_f32 v90, v94, v95
	v_mov_b64_e32 v[94:95], s[34:35]
	v_ashrrev_i32_e32 v98, 4, v99
	v_mad_i64_i32 v[94:95], s[34:35], v99, s68, v[94:95]
	v_add_u32_e32 v98, 0xffffc000, v98
	v_lshl_add_u64 v[94:95], v[138:139], 1, v[94:95]
	s_and_b64 vcc, exec, s[10:11]
	v_cvt_pk_bf16_f32 v91, v96, v97
	v_cvt_pk_bf16_f32 v92, v92, v93
	v_cvt_pk_bf16_f32 v93, v100, v101
	s_mov_b64 exec, s[78:79]
	global_store_dwordx4 v[94:95], v[90:93], off nt
	s_mov_b64 exec, s[80:81]
	global_store_dwordx4 v[94:95], v[90:93], off
	s_mov_b64 exec, -1
	s_cbranch_vccnz .LBB0_177
	v_lshl_add_u32 v96, s30, 10, v98
	v_ashrrev_i32_e32 v97, 31, v96
	v_lshlrev_b64 v[96:97], 12, v[96:97]
	v_lshl_add_u64 v[96:97], v[206:207], 0, v[96:97]
	global_store_dwordx4 v[96:97], v[90:93], off
.LBB0_177:
	v_cvt_f32_i32_e32 v83, v83
	v_cvt_f32_i32_e32 v85, v85
	v_cvt_f32_i32_e32 v84, v84
	v_cvt_f32_i32_e32 v82, v82
	v_cvt_f32_i32_e32 v87, v87
	v_cvt_f32_i32_e32 v86, v86
	v_cvt_f32_i32_e32 v89, v89
	v_cvt_f32_i32_e32 v88, v88
	v_mov_b32_e32 v161, v160
	v_mov_b32_e32 v90, v160
	v_mov_b32_e32 v91, v160
	v_pk_mul_f32 v[92:93], v[90:91], v[124:125]
	v_pk_mul_f32 v[90:91], v[90:91], v[122:123]
	v_pk_mul_f32 v[100:101], v[160:161], v[128:129]
	v_pk_mul_f32 v[96:97], v[160:161], v[126:127]
	v_pk_mul_f32 v[90:91], v[90:91], v[84:85]
	v_pk_mul_f32 v[84:85], v[100:101], v[82:83]
	s_and_b64 vcc, exec, s[10:11]
	v_pk_mul_f32 v[88:89], v[92:93], v[88:89]
	v_pk_mul_f32 v[86:87], v[96:97], v[86:87]
	s_nop 0
	v_cvt_pk_bf16_f32 v82, v86, v87
	v_cvt_pk_bf16_f32 v83, v88, v89
	v_cvt_pk_bf16_f32 v84, v84, v85
	v_cvt_pk_bf16_f32 v85, v90, v91
	s_mov_b64 exec, s[78:79]
	global_store_dwordx4 v[94:95], v[82:85], off offset:256 nt
	s_mov_b64 exec, s[80:81]
	global_store_dwordx4 v[94:95], v[82:85], off offset:256
	s_mov_b64 exec, -1
	s_cbranch_vccnz .LBB0_179
	v_add_u32_e32 v86, v98, v118
	v_ashrrev_i32_e32 v87, 31, v86
	v_lshlrev_b64 v[86:87], 12, v[86:87]
	v_lshl_add_u64 v[86:87], v[206:207], 0, v[86:87]
	global_store_dwordx4 v[86:87], v[82:85], off
.LBB0_179:
	v_cvt_f32_i32_e32 v79, v79
	v_cvt_f32_i32_e32 v78, v78
	v_cvt_f32_i32_e32 v81, v81
	v_cvt_f32_i32_e32 v80, v80
	v_cvt_f32_i32_e32 v75, v75
	v_cvt_f32_i32_e32 v77, v77
	v_cvt_f32_i32_e32 v76, v76
	v_cvt_f32_i32_e32 v74, v74
	v_pk_mul_f32 v[86:87], v[158:159], v[150:151] op_sel_hi:[0,1]
	v_readlane_b32 s34, v245, 9
	v_pk_mul_f32 v[84:85], v[158:159], v[148:149] op_sel_hi:[0,1]
	v_pk_mul_f32 v[88:89], v[158:159], v[144:145] op_sel_hi:[0,1]
	v_pk_mul_f32 v[90:91], v[158:159], v[146:147] op_sel_hi:[0,1]
	v_pk_mul_f32 v[78:79], v[86:87], v[78:79]
	v_readlane_b32 s35, v245, 10
	v_or_b32_e32 v83, 48, v156
	v_pk_mul_f32 v[80:81], v[84:85], v[80:81]
	v_pk_mul_f32 v[84:85], v[88:89], v[76:77]
	v_pk_mul_f32 v[76:77], v[90:91], v[74:75]
	v_cvt_pk_bf16_f32 v74, v78, v79
	v_mov_b64_e32 v[78:79], s[34:35]
	v_ashrrev_i32_e32 v82, 4, v83
	v_mad_i64_i32 v[78:79], s[34:35], v83, s68, v[78:79]
	v_add_u32_e32 v82, 0xffffc000, v82
	v_lshl_add_u64 v[78:79], v[138:139], 1, v[78:79]
	s_and_b64 vcc, exec, s[10:11]
	v_cvt_pk_bf16_f32 v75, v80, v81
	v_cvt_pk_bf16_f32 v76, v76, v77
	v_cvt_pk_bf16_f32 v77, v84, v85
	s_mov_b64 exec, s[78:79]
	global_store_dwordx4 v[78:79], v[74:77], off nt
	s_mov_b64 exec, s[80:81]
	global_store_dwordx4 v[78:79], v[74:77], off
	s_mov_b64 exec, -1
	s_cbranch_vccnz .LBB0_181
	v_lshl_add_u32 v80, s30, 10, v82
	v_ashrrev_i32_e32 v81, 31, v80
	v_lshlrev_b64 v[80:81], 12, v[80:81]
	v_lshl_add_u64 v[80:81], v[206:207], 0, v[80:81]
	global_store_dwordx4 v[80:81], v[74:77], off
;     __device__ __forceinline__ void operator()(const f32x4 (&acc)[2][2][4][2], const Unit& u, int wr, int wc, int fr, int fq) const {
;     ...
;         for (int kb = 0; kb < 8; ++kb) { const int ai = kb >> 2, m = kb & 3;
;             if (kb < 7) EPB_LOAD(kb + 1);
;             { const int row = row0 + ai * HALF + m * 16; float rmx = 0.f;
; #pragma unroll
;                 for (int bj = 0; bj < 2; ++bj) { const int col = col0 + bj * HALF; f32x4 v0 = acc[ai][bj][m][0], v1 = acc[ai][bj][m][1];
;                     if (QI8) { const f32x4 c0 = cb[bj][0] * ra[ai][m], c1 = cb[bj][1] * ra[ai][m]; const i32x4 i0 = __builtin_bit_cast(i32x4, v0), i1 = __builtin_bit_cast(i32x4, v1);
;                         v0 = (f32x4){(float)i0[0], (float)i0[1], (float)i0[2], (float)i0[3]} * c0; v1 = (f32x4){(float)i1[0], (float)i1[1], (float)i1[2], (float)i1[3]} * c1; }
;                     else if (MODE == 0) { v0 = v0 * tsc; v1 = v1 * tsc; }
;                     if (!QI8 && MODE == 1) { v0 = v0 * cb[bj][0]; v1 = v1 * cb[bj][1]; }
;                     if (MODE == 2 || MODE == 3) { const u32x4 g = gq[kb & 1][bj];
;                         f32x4 g0 = {sigmoidf_(bflo(g.x)), sigmoidf_(bfhi(g.x)), sigmoidf_(bflo(g.y)), sigmoidf_(bfhi(g.y))};
;                         f32x4 g1 = {sigmoidf_(bflo(g.z)), sigmoidf_(bfhi(g.z)), sigmoidf_(bflo(g.w)), sigmoidf_(bfhi(g.w))};
;                         v0 = v0 * g0; v1 = v1 * g1;
;                         if (MODE == 3) { const u32x4 q = aq[kb & 1][bj];
;                             v0 = v0 + (f32x4){bflo(q.x), bfhi(q.x), bflo(q.y), bfhi(q.y)}; v1 = v1 + (f32x4){bflo(q.z), bfhi(q.z), bflo(q.w), bfhi(q.w)}; } }
;                     if (MODE == 4) { v0 = v0 + rs[kb & 1][bj][0]; v1 = v1 + rs[kb & 1][bj][1]; }
;                     if (MODE == 5) { const u32x4 c = gq[kb & 1][bj], q = aq[kb & 1][bj];
;                         v0 = (f32x4){bflo(c.x) + sigmoidf_(v0[0]) * bflo(q.x), bfhi(c.x) + sigmoidf_(v0[1]) * bfhi(q.x), bflo(c.y) + sigmoidf_(v0[2]) * bflo(q.y), bfhi(c.y) + sigmoidf_(v0[3]) * bfhi(q.y)};
;                         v1 = (f32x4){bflo(c.z) + sigmoidf_(v1[0]) * bflo(q.z), bfhi(c.z) + sigmoidf_(v1[1]) * bfhi(q.z), bflo(c.w) + sigmoidf_(v1[2]) * bflo(q.w), bfhi(c.w) + sigmoidf_(v1[3]) * bfhi(q.w)}; }
;                     u32x4 w; w.x = cvtpk(v0[0], v0[1]); w.y = cvtpk(v0[2], v0[3]); w.z = cvtpk(v1[0], v1[1]); w.w = cvtpk(v1[2], v1[3]);
.LBB0_181:
	v_cvt_f32_i32_e32 v67, v67
	v_cvt_f32_i32_e32 v69, v69
	v_cvt_f32_i32_e32 v68, v68
	v_cvt_f32_i32_e32 v66, v66
	v_cvt_f32_i32_e32 v71, v71
	v_cvt_f32_i32_e32 v70, v70
	v_cvt_f32_i32_e32 v73, v73
	v_cvt_f32_i32_e32 v72, v72
	v_mov_b32_e32 v159, v158
	v_mov_b32_e32 v74, v158
	v_mov_b32_e32 v75, v158
	v_pk_mul_f32 v[76:77], v[74:75], v[124:125]
	v_pk_mul_f32 v[74:75], v[74:75], v[122:123]
	v_pk_mul_f32 v[84:85], v[158:159], v[128:129]
	v_pk_mul_f32 v[80:81], v[158:159], v[126:127]
	v_pk_mul_f32 v[74:75], v[74:75], v[68:69]
	v_pk_mul_f32 v[68:69], v[84:85], v[66:67]
	s_and_b64 vcc, exec, s[10:11]
	v_pk_mul_f32 v[72:73], v[76:77], v[72:73]
	v_pk_mul_f32 v[70:71], v[80:81], v[70:71]
	s_nop 0
	v_cvt_pk_bf16_f32 v66, v70, v71
	v_cvt_pk_bf16_f32 v67, v72, v73
	v_cvt_pk_bf16_f32 v68, v68, v69
	v_cvt_pk_bf16_f32 v69, v74, v75
	s_mov_b64 exec, s[78:79]
	global_store_dwordx4 v[78:79], v[66:69], off offset:256 nt
	s_mov_b64 exec, s[80:81]
	global_store_dwordx4 v[78:79], v[66:69], off offset:256
	s_mov_b64 exec, -1
	s_cbranch_vccnz .LBB0_183
	v_add_u32_e32 v70, v82, v118
	v_ashrrev_i32_e32 v71, 31, v70
	v_lshlrev_b64 v[70:71], 12, v[70:71]
	v_lshl_add_u64 v[70:71], v[206:207], 0, v[70:71]
	global_store_dwordx4 v[70:71], v[66:69], off
.LBB0_183:
	v_cvt_f32_i32_e32 v63, v63
	v_cvt_f32_i32_e32 v62, v62
	v_cvt_f32_i32_e32 v65, v65
	v_cvt_f32_i32_e32 v64, v64
	v_cvt_f32_i32_e32 v59, v59
	v_cvt_f32_i32_e32 v61, v61
	v_cvt_f32_i32_e32 v60, v60
	v_cvt_f32_i32_e32 v58, v58
	v_pk_mul_f32 v[70:71], v[154:155], v[150:151] op_sel_hi:[0,1]
	v_readlane_b32 s34, v245, 9
	v_pk_mul_f32 v[68:69], v[154:155], v[148:149] op_sel_hi:[0,1]
	v_pk_mul_f32 v[72:73], v[154:155], v[144:145] op_sel_hi:[0,1]
	v_pk_mul_f32 v[74:75], v[154:155], v[146:147] op_sel_hi:[0,1]
	v_pk_mul_f32 v[62:63], v[70:71], v[62:63]
	v_readlane_b32 s35, v245, 10
	v_add_u32_e32 v66, 0x80, v156
	v_pk_mul_f32 v[64:65], v[68:69], v[64:65]
	v_pk_mul_f32 v[68:69], v[72:73], v[60:61]
	v_pk_mul_f32 v[60:61], v[74:75], v[58:59]
	v_cvt_pk_bf16_f32 v58, v62, v63
	v_mov_b64_e32 v[62:63], s[34:35]
	v_ashrrev_i32_e32 v67, 4, v66
	v_mad_i64_i32 v[62:63], s[34:35], v66, s68, v[62:63]
	v_add_u32_e32 v67, 0xffffc000, v67
	v_lshl_add_u64 v[62:63], v[138:139], 1, v[62:63]
	s_and_b64 vcc, exec, s[10:11]
	v_cvt_pk_bf16_f32 v59, v64, v65
	v_cvt_pk_bf16_f32 v60, v60, v61
	v_cvt_pk_bf16_f32 v61, v68, v69
	s_mov_b64 exec, s[78:79]
	global_store_dwordx4 v[62:63], v[58:61], off nt
	s_mov_b64 exec, s[80:81]
	global_store_dwordx4 v[62:63], v[58:61], off
	s_mov_b64 exec, -1
	s_cbranch_vccnz .LBB0_185
	v_lshl_add_u32 v64, s30, 10, v67
	v_ashrrev_i32_e32 v65, 31, v64
	v_lshlrev_b64 v[64:65], 12, v[64:65]
	v_lshl_add_u64 v[64:65], v[206:207], 0, v[64:65]
	global_store_dwordx4 v[64:65], v[58:61], off
.LBB0_185:
	v_cvt_f32_i32_e32 v51, v51
	v_cvt_f32_i32_e32 v53, v53
	v_cvt_f32_i32_e32 v52, v52
	v_cvt_f32_i32_e32 v50, v50
	v_cvt_f32_i32_e32 v55, v55
	v_cvt_f32_i32_e32 v54, v54
	v_cvt_f32_i32_e32 v57, v57
	v_cvt_f32_i32_e32 v56, v56
	v_mov_b32_e32 v155, v154
	v_mov_b32_e32 v58, v154
	v_mov_b32_e32 v59, v154
	v_pk_mul_f32 v[60:61], v[58:59], v[124:125]
	v_pk_mul_f32 v[58:59], v[58:59], v[122:123]
	v_pk_mul_f32 v[68:69], v[154:155], v[128:129]
	v_pk_mul_f32 v[64:65], v[154:155], v[126:127]
	v_pk_mul_f32 v[58:59], v[58:59], v[52:53]
	v_pk_mul_f32 v[52:53], v[68:69], v[50:51]
	s_and_b64 vcc, exec, s[10:11]
	v_pk_mul_f32 v[56:57], v[60:61], v[56:57]
	v_pk_mul_f32 v[54:55], v[64:65], v[54:55]
	s_nop 0
	v_cvt_pk_bf16_f32 v50, v54, v55
	v_cvt_pk_bf16_f32 v51, v56, v57
	v_cvt_pk_bf16_f32 v52, v52, v53
	v_cvt_pk_bf16_f32 v53, v58, v59
	s_mov_b64 exec, s[78:79]
	global_store_dwordx4 v[62:63], v[50:53], off offset:256 nt
	s_mov_b64 exec, s[80:81]
	global_store_dwordx4 v[62:63], v[50:53], off offset:256
	s_mov_b64 exec, -1
	s_cbranch_vccnz .LBB0_187
	v_add_u32_e32 v54, v67, v118
	v_ashrrev_i32_e32 v55, 31, v54
	v_lshlrev_b64 v[54:55], 12, v[54:55]
	v_lshl_add_u64 v[54:55], v[206:207], 0, v[54:55]
	global_store_dwordx4 v[54:55], v[50:53], off
.LBB0_187:
	v_cvt_f32_i32_e32 v47, v47
	v_cvt_f32_i32_e32 v46, v46
	v_cvt_f32_i32_e32 v49, v49
	v_cvt_f32_i32_e32 v48, v48
	v_cvt_f32_i32_e32 v43, v43
	v_cvt_f32_i32_e32 v45, v45
	v_cvt_f32_i32_e32 v44, v44
	v_cvt_f32_i32_e32 v42, v42
	v_pk_mul_f32 v[54:55], v[152:153], v[150:151] op_sel_hi:[0,1]
	v_readlane_b32 s34, v245, 9
	v_pk_mul_f32 v[52:53], v[152:153], v[148:149] op_sel_hi:[0,1]
	v_pk_mul_f32 v[56:57], v[152:153], v[144:145] op_sel_hi:[0,1]
	v_pk_mul_f32 v[58:59], v[152:153], v[146:147] op_sel_hi:[0,1]
	v_pk_mul_f32 v[46:47], v[54:55], v[46:47]
	v_readlane_b32 s35, v245, 10
	v_or_b32_e32 v51, 16, v66
	v_pk_mul_f32 v[48:49], v[52:53], v[48:49]
	v_pk_mul_f32 v[52:53], v[56:57], v[44:45]
	v_pk_mul_f32 v[44:45], v[58:59], v[42:43]
	v_cvt_pk_bf16_f32 v42, v46, v47
	v_mov_b64_e32 v[46:47], s[34:35]
	v_ashrrev_i32_e32 v50, 4, v51
	v_mad_i64_i32 v[46:47], s[34:35], v51, s68, v[46:47]
	v_add_u32_e32 v50, 0xffffc000, v50
	v_lshl_add_u64 v[46:47], v[138:139], 1, v[46:47]
	s_and_b64 vcc, exec, s[10:11]
	v_cvt_pk_bf16_f32 v43, v48, v49
	v_cvt_pk_bf16_f32 v44, v44, v45
	v_cvt_pk_bf16_f32 v45, v52, v53
	s_mov_b64 exec, s[78:79]
	global_store_dwordx4 v[46:47], v[42:45], off nt
	s_mov_b64 exec, s[80:81]
	global_store_dwordx4 v[46:47], v[42:45], off
	s_mov_b64 exec, -1
	s_cbranch_vccnz .LBB0_189
	v_lshl_add_u32 v48, s30, 10, v50
	v_ashrrev_i32_e32 v49, 31, v48
	v_lshlrev_b64 v[48:49], 12, v[48:49]
	v_lshl_add_u64 v[48:49], v[206:207], 0, v[48:49]
	global_store_dwordx4 v[48:49], v[42:45], off
;     __device__ __forceinline__ void operator()(const f32x4 (&acc)[2][2][4][2], const Unit& u, int wr, int wc, int fr, int fq) const {
;     ...
;         for (int kb = 0; kb < 8; ++kb) { const int ai = kb >> 2, m = kb & 3;
;             if (kb < 7) EPB_LOAD(kb + 1);
;             { const int row = row0 + ai * HALF + m * 16; float rmx = 0.f;
; #pragma unroll
;                 for (int bj = 0; bj < 2; ++bj) { const int col = col0 + bj * HALF; f32x4 v0 = acc[ai][bj][m][0], v1 = acc[ai][bj][m][1];
;                     if (QI8) { const f32x4 c0 = cb[bj][0] * ra[ai][m], c1 = cb[bj][1] * ra[ai][m]; const i32x4 i0 = __builtin_bit_cast(i32x4, v0), i1 = __builtin_bit_cast(i32x4, v1);
;                         v0 = (f32x4){(float)i0[0], (float)i0[1], (float)i0[2], (float)i0[3]} * c0; v1 = (f32x4){(float)i1[0], (float)i1[1], (float)i1[2], (float)i1[3]} * c1; }
;                     else if (MODE == 0) { v0 = v0 * tsc; v1 = v1 * tsc; }
;                     if (!QI8 && MODE == 1) { v0 = v0 * cb[bj][0]; v1 = v1 * cb[bj][1]; }
;                     if (MODE == 2 || MODE == 3) { const u32x4 g = gq[kb & 1][bj];
;                         f32x4 g0 = {sigmoidf_(bflo(g.x)), sigmoidf_(bfhi(g.x)), sigmoidf_(bflo(g.y)), sigmoidf_(bfhi(g.y))};
;                         f32x4 g1 = {sigmoidf_(bflo(g.z)), sigmoidf_(bfhi(g.z)), sigmoidf_(bflo(g.w)), sigmoidf_(bfhi(g.w))};
;                         v0 = v0 * g0; v1 = v1 * g1;
;                         if (MODE == 3) { const u32x4 q = aq[kb & 1][bj];
;                             v0 = v0 + (f32x4){bflo(q.x), bfhi(q.x), bflo(q.y), bfhi(q.y)}; v1 = v1 + (f32x4){bflo(q.z), bfhi(q.z), bflo(q.w), bfhi(q.w)}; } }
;                     if (MODE == 4) { v0 = v0 + rs[kb & 1][bj][0]; v1 = v1 + rs[kb & 1][bj][1]; }
;                     if (MODE == 5) { const u32x4 c = gq[kb & 1][bj], q = aq[kb & 1][bj];
;                         v0 = (f32x4){bflo(c.x) + sigmoidf_(v0[0]) * bflo(q.x), bfhi(c.x) + sigmoidf_(v0[1]) * bfhi(q.x), bflo(c.y) + sigmoidf_(v0[2]) * bflo(q.y), bfhi(c.y) + sigmoidf_(v0[3]) * bfhi(q.y)};
;                         v1 = (f32x4){bflo(c.z) + sigmoidf_(v1[0]) * bflo(q.z), bfhi(c.z) + sigmoidf_(v1[1]) * bfhi(q.z), bflo(c.w) + sigmoidf_(v1[2]) * bflo(q.w), bfhi(c.w) + sigmoidf_(v1[3]) * bfhi(q.w)}; }
;                     u32x4 w; w.x = cvtpk(v0[0], v0[1]); w.y = cvtpk(v0[2], v0[3]); w.z = cvtpk(v1[0], v1[1]); w.w = cvtpk(v1[2], v1[3]);
.LBB0_189:
	v_cvt_f32_i32_e32 v35, v35
	v_cvt_f32_i32_e32 v37, v37
	v_cvt_f32_i32_e32 v36, v36
	v_cvt_f32_i32_e32 v34, v34
	v_cvt_f32_i32_e32 v39, v39
	v_cvt_f32_i32_e32 v38, v38
	v_cvt_f32_i32_e32 v41, v41
	v_cvt_f32_i32_e32 v40, v40
	v_mov_b32_e32 v153, v152
	v_mov_b32_e32 v42, v152
	v_mov_b32_e32 v43, v152
	v_pk_mul_f32 v[44:45], v[42:43], v[124:125]
	v_pk_mul_f32 v[42:43], v[42:43], v[122:123]
	v_pk_mul_f32 v[52:53], v[152:153], v[128:129]
	v_pk_mul_f32 v[48:49], v[152:153], v[126:127]
	v_pk_mul_f32 v[42:43], v[42:43], v[36:37]
	v_pk_mul_f32 v[36:37], v[52:53], v[34:35]
	s_and_b64 vcc, exec, s[10:11]
	v_pk_mul_f32 v[40:41], v[44:45], v[40:41]
	v_pk_mul_f32 v[38:39], v[48:49], v[38:39]
	s_nop 0
	v_cvt_pk_bf16_f32 v34, v38, v39
	v_cvt_pk_bf16_f32 v35, v40, v41
	v_cvt_pk_bf16_f32 v36, v36, v37
	v_cvt_pk_bf16_f32 v37, v42, v43
	s_mov_b64 exec, s[78:79]
	global_store_dwordx4 v[46:47], v[34:37], off offset:256 nt
	s_mov_b64 exec, s[80:81]
	global_store_dwordx4 v[46:47], v[34:37], off offset:256
	s_mov_b64 exec, -1
	s_cbranch_vccnz .LBB0_191
	v_add_u32_e32 v38, v50, v118
	v_ashrrev_i32_e32 v39, 31, v38
	v_lshlrev_b64 v[38:39], 12, v[38:39]
	v_lshl_add_u64 v[38:39], v[206:207], 0, v[38:39]
	global_store_dwordx4 v[38:39], v[34:37], off
.LBB0_191:
	v_cvt_f32_i32_e32 v31, v31
	v_cvt_f32_i32_e32 v30, v30
	v_cvt_f32_i32_e32 v33, v33
	v_cvt_f32_i32_e32 v32, v32
	v_cvt_f32_i32_e32 v27, v27
	v_cvt_f32_i32_e32 v29, v29
	v_cvt_f32_i32_e32 v28, v28
	v_cvt_f32_i32_e32 v26, v26
	v_pk_mul_f32 v[38:39], v[142:143], v[150:151] op_sel_hi:[0,1]
	v_readlane_b32 s34, v245, 9
	v_pk_mul_f32 v[36:37], v[142:143], v[148:149] op_sel_hi:[0,1]
	v_pk_mul_f32 v[40:41], v[142:143], v[144:145] op_sel_hi:[0,1]
	v_pk_mul_f32 v[42:43], v[142:143], v[146:147] op_sel_hi:[0,1]
	v_pk_mul_f32 v[30:31], v[38:39], v[30:31]
	v_readlane_b32 s35, v245, 10
	v_or_b32_e32 v35, 32, v66
	v_pk_mul_f32 v[32:33], v[36:37], v[32:33]
	v_pk_mul_f32 v[36:37], v[40:41], v[28:29]
	v_pk_mul_f32 v[28:29], v[42:43], v[26:27]
	v_cvt_pk_bf16_f32 v26, v30, v31
	v_mov_b64_e32 v[30:31], s[34:35]
	v_ashrrev_i32_e32 v34, 4, v35
	v_mad_i64_i32 v[30:31], s[34:35], v35, s68, v[30:31]
	v_add_u32_e32 v34, 0xffffc000, v34
	v_lshl_add_u64 v[30:31], v[138:139], 1, v[30:31]
	s_and_b64 vcc, exec, s[10:11]
	v_cvt_pk_bf16_f32 v27, v32, v33
	v_cvt_pk_bf16_f32 v28, v28, v29
	v_cvt_pk_bf16_f32 v29, v36, v37
	s_mov_b64 exec, s[78:79]
	global_store_dwordx4 v[30:31], v[26:29], off nt
	s_mov_b64 exec, s[80:81]
	global_store_dwordx4 v[30:31], v[26:29], off
	s_mov_b64 exec, -1
	s_cbranch_vccnz .LBB0_193
	v_lshl_add_u32 v32, s30, 10, v34
	v_ashrrev_i32_e32 v33, 31, v32
	v_lshlrev_b64 v[32:33], 12, v[32:33]
	v_lshl_add_u64 v[32:33], v[206:207], 0, v[32:33]
	global_store_dwordx4 v[32:33], v[26:29], off
.LBB0_193:
	v_cvt_f32_i32_e32 v19, v19
	v_cvt_f32_i32_e32 v21, v21
	v_cvt_f32_i32_e32 v20, v20
	v_cvt_f32_i32_e32 v18, v18
	v_cvt_f32_i32_e32 v23, v23
	v_cvt_f32_i32_e32 v22, v22
	v_cvt_f32_i32_e32 v25, v25
	v_cvt_f32_i32_e32 v24, v24
	v_mov_b32_e32 v143, v142
	v_mov_b32_e32 v26, v142
	v_mov_b32_e32 v27, v142
	v_pk_mul_f32 v[28:29], v[26:27], v[124:125]
	v_pk_mul_f32 v[26:27], v[26:27], v[122:123]
	v_pk_mul_f32 v[36:37], v[142:143], v[128:129]
	v_pk_mul_f32 v[32:33], v[142:143], v[126:127]
	v_pk_mul_f32 v[26:27], v[26:27], v[20:21]
	v_pk_mul_f32 v[20:21], v[36:37], v[18:19]
	s_and_b64 vcc, exec, s[10:11]
	v_pk_mul_f32 v[24:25], v[28:29], v[24:25]
	v_pk_mul_f32 v[22:23], v[32:33], v[22:23]
	s_nop 0
	v_cvt_pk_bf16_f32 v18, v22, v23
	v_cvt_pk_bf16_f32 v19, v24, v25
	v_cvt_pk_bf16_f32 v20, v20, v21
	v_cvt_pk_bf16_f32 v21, v26, v27
	s_mov_b64 exec, s[78:79]
	global_store_dwordx4 v[30:31], v[18:21], off offset:256 nt
	s_mov_b64 exec, s[80:81]
	global_store_dwordx4 v[30:31], v[18:21], off offset:256
	s_mov_b64 exec, -1
	s_cbranch_vccnz .LBB0_195
	v_add_u32_e32 v22, v34, v118
	v_ashrrev_i32_e32 v23, 31, v22
	v_lshlrev_b64 v[22:23], 12, v[22:23]
	v_lshl_add_u64 v[22:23], v[206:207], 0, v[22:23]
	global_store_dwordx4 v[22:23], v[18:21], off
.LBB0_195:
	v_cvt_f32_i32_e32 v15, v15
	v_cvt_f32_i32_e32 v14, v14
	v_cvt_f32_i32_e32 v17, v17
	v_cvt_f32_i32_e32 v16, v16
	v_cvt_f32_i32_e32 v11, v11
	v_cvt_f32_i32_e32 v13, v13
	v_cvt_f32_i32_e32 v12, v12
	v_cvt_f32_i32_e32 v10, v10
	v_pk_mul_f32 v[22:23], v[140:141], v[150:151] op_sel_hi:[0,1]
	v_readlane_b32 s34, v245, 9
	v_pk_mul_f32 v[20:21], v[140:141], v[148:149] op_sel_hi:[0,1]
	v_pk_mul_f32 v[24:25], v[140:141], v[144:145] op_sel_hi:[0,1]
	v_pk_mul_f32 v[26:27], v[140:141], v[146:147] op_sel_hi:[0,1]
	v_pk_mul_f32 v[14:15], v[22:23], v[14:15]
	v_readlane_b32 s35, v245, 10
	v_or_b32_e32 v19, 48, v66
	v_pk_mul_f32 v[16:17], v[20:21], v[16:17]
	v_pk_mul_f32 v[20:21], v[24:25], v[12:13]
	v_pk_mul_f32 v[12:13], v[26:27], v[10:11]
	v_cvt_pk_bf16_f32 v10, v14, v15
	v_mov_b64_e32 v[14:15], s[34:35]
	v_ashrrev_i32_e32 v18, 4, v19
	v_mad_i64_i32 v[14:15], s[34:35], v19, s68, v[14:15]
	v_add_u32_e32 v18, 0xffffc000, v18
	v_lshl_add_u64 v[14:15], v[138:139], 1, v[14:15]
	s_and_b64 vcc, exec, s[10:11]
	v_cvt_pk_bf16_f32 v11, v16, v17
	v_cvt_pk_bf16_f32 v12, v12, v13
	v_cvt_pk_bf16_f32 v13, v20, v21
	s_mov_b64 exec, s[78:79]
	global_store_dwordx4 v[14:15], v[10:13], off nt
	s_mov_b64 exec, s[80:81]
	global_store_dwordx4 v[14:15], v[10:13], off
	s_mov_b64 exec, -1
	s_cbranch_vccnz .LBB0_197
	v_lshl_add_u32 v16, s30, 10, v18
	v_ashrrev_i32_e32 v17, 31, v16
	v_lshlrev_b64 v[16:17], 12, v[16:17]
	v_lshl_add_u64 v[16:17], v[206:207], 0, v[16:17]
	global_store_dwordx4 v[16:17], v[10:13], off
.LBB0_197:
	v_cvt_f32_i32_e32 v3, v3
	v_cvt_f32_i32_e32 v5, v5
	v_cvt_f32_i32_e32 v4, v4
	v_cvt_f32_i32_e32 v2, v2
	v_cvt_f32_i32_e32 v7, v7
	v_cvt_f32_i32_e32 v6, v6
	v_cvt_f32_i32_e32 v9, v9
	v_cvt_f32_i32_e32 v8, v8
	v_mov_b32_e32 v141, v140
	v_mov_b32_e32 v10, v140
	v_mov_b32_e32 v11, v140
	v_pk_mul_f32 v[12:13], v[10:11], v[124:125]
	v_pk_mul_f32 v[10:11], v[10:11], v[122:123]
	v_pk_mul_f32 v[20:21], v[140:141], v[128:129]
	v_pk_mul_f32 v[16:17], v[140:141], v[126:127]
	v_pk_mul_f32 v[10:11], v[10:11], v[4:5]
	v_pk_mul_f32 v[4:5], v[20:21], v[2:3]
	s_and_b64 vcc, exec, s[10:11]
	v_pk_mul_f32 v[8:9], v[12:13], v[8:9]
	v_pk_mul_f32 v[6:7], v[16:17], v[6:7]
	s_nop 0
	v_cvt_pk_bf16_f32 v2, v6, v7
	v_cvt_pk_bf16_f32 v3, v8, v9
	v_cvt_pk_bf16_f32 v4, v4, v5
	v_cvt_pk_bf16_f32 v5, v10, v11
	s_mov_b64 exec, s[78:79]
	global_store_dwordx4 v[14:15], v[2:5], off offset:256 nt
	s_mov_b64 exec, s[80:81]
	global_store_dwordx4 v[14:15], v[2:5], off offset:256
	s_mov_b64 exec, -1
	s_cbranch_vccnz .LBB0_199
	v_add_u32_e32 v6, v18, v118
	v_ashrrev_i32_e32 v7, 31, v6
	v_lshlrev_b64 v[6:7], 12, v[6:7]
	v_lshl_add_u64 v[6:7], v[206:207], 0, v[6:7]
	global_store_dwordx4 v[6:7], v[2:5], off
